# baseline (speedup 1.0000x reference)
.LBB0_23:
	v_mov_b32_e32 v237, v48
	s_branch .LBB0_24
	.p2align	6
